# v37
# speedup vs baseline: 1.0037x; 1.0037x over previous
.LBB1_20:
	s_waitcnt lgkmcnt(0)
	s_barrier
	v_mfma_f32_16x16x32_f16 v[64:67], v[148:151], v[188:191], v[64:67]
	v_mfma_f32_16x16x32_f16 v[64:67], v[152:155], v[192:195], v[64:67]
	v_mfma_f32_16x16x32_f16 v[56:59], v[160:163], v[192:195], v[56:59]
	v_mfma_f32_16x16x32_f16 v[56:59], v[156:159], v[188:191], v[56:59]
	v_mfma_f32_16x16x32_f16 v[40:43], v[156:159], v[176:179], v[40:43]
	v_mfma_f32_16x16x32_f16 v[40:43], v[160:163], v[180:183], v[40:43]
	v_mfma_f32_16x16x32_f16 v[48:51], v[152:155], v[180:183], v[48:51]
	v_mfma_f32_16x16x32_f16 v[48:51], v[148:151], v[176:179], v[48:51]
	v_mfma_f32_16x16x32_f16 v[32:35], v[148:151], v[172:175], v[32:35]
	v_mfma_f32_16x16x32_f16 v[32:35], v[152:155], v[184:187], v[32:35]
	v_mfma_f32_16x16x32_f16 v[24:27], v[160:163], v[184:187], v[24:27]
	v_mfma_f32_16x16x32_f16 v[24:27], v[156:159], v[172:175], v[24:27]
	v_mfma_f32_16x16x32_f16 v[8:11], v[156:159], v[164:167], v[8:11]
	v_mfma_f32_16x16x32_f16 v[8:11], v[160:163], v[168:171], v[8:11]
	v_mfma_f32_16x16x32_f16 v[16:19], v[152:155], v[168:171], v[16:19]
	v_mfma_f32_16x16x32_f16 v[16:19], v[148:151], v[164:167], v[16:19]
	v_mfma_f32_16x16x32_f16 v[60:63], v[132:135], v[188:191], v[60:63]
	v_mfma_f32_16x16x32_f16 v[60:63], v[136:139], v[192:195], v[60:63]
	v_mfma_f32_16x16x32_f16 v[52:55], v[144:147], v[192:195], v[52:55]
	v_mfma_f32_16x16x32_f16 v[52:55], v[140:143], v[188:191], v[52:55]
	v_mfma_f32_16x16x32_f16 v[36:39], v[140:143], v[176:179], v[36:39]
	v_mfma_f32_16x16x32_f16 v[36:39], v[144:147], v[180:183], v[36:39]
	v_mfma_f32_16x16x32_f16 v[44:47], v[136:139], v[180:183], v[44:47]
	v_mfma_f32_16x16x32_f16 v[44:47], v[132:135], v[176:179], v[44:47]
	v_mfma_f32_16x16x32_f16 v[28:31], v[132:135], v[172:175], v[28:31]
	v_mfma_f32_16x16x32_f16 v[28:31], v[136:139], v[184:187], v[28:31]
	v_mfma_f32_16x16x32_f16 v[20:23], v[144:147], v[184:187], v[20:23]
	v_mfma_f32_16x16x32_f16 v[20:23], v[140:143], v[172:175], v[20:23]
	v_mfma_f32_16x16x32_f16 v[4:7], v[140:143], v[164:167], v[4:7]
	v_mfma_f32_16x16x32_f16 v[4:7], v[144:147], v[168:171], v[4:7]
	v_mfma_f32_16x16x32_f16 v[12:15], v[136:139], v[168:171], v[12:15]
	v_mfma_f32_16x16x32_f16 v[12:15], v[132:135], v[164:167], v[12:15]
	s_barrier
	s_add_u32 s48, s48, 0x100000
	ds_read_b128 v[148:151], v228 offset:32768
	ds_read_b128 v[152:155], v229 offset:32768
	s_addc_u32 s49, s49, 0
	s_mov_b32 m0, s57
	ds_read_b128 v[156:159], v228 offset:34816
	ds_read_b128 v[160:163], v229 offset:34816
	ds_read_b128 v[132:135], v228 offset:49152
	ds_read_b128 v[136:139], v229 offset:49152
	ds_read_b128 v[140:143], v228 offset:51200
	ds_read_b128 v[144:147], v229 offset:51200
	ds_read_b128 v[188:191], v226 offset:32768
	ds_read_b128 v[176:179], v226 offset:34816
	ds_read_b128 v[192:195], v227 offset:32768
	ds_read_b128 v[180:183], v227 offset:34816
	ds_read_b128 v[172:175], v226 offset:36864
	ds_read_b128 v[164:167], v226 offset:38912
	ds_read_b128 v[184:187], v227 offset:36864
	ds_read_b128 v[168:171], v227 offset:38912
	global_load_lds_dwordx4 v202, s[48:49] sc1
	s_mov_b32 m0, s58
	s_nop 0
	global_load_lds_dwordx4 v198, s[48:49] sc1
	s_mov_b64 s[48:49], -1
	s_mov_b64 vcc, s[4:5]
	s_cbranch_vccz .LBB1_22
	s_waitcnt vmcnt(8)
	s_mov_b64 s[48:49], 0

.LBB1_24:
	s_waitcnt lgkmcnt(0)
	s_barrier
	v_mfma_f32_16x16x32_f16 v[128:131], v[148:151], v[188:191], v[128:131]
	v_mfma_f32_16x16x32_f16 v[128:131], v[152:155], v[192:195], v[128:131]
	v_mfma_f32_16x16x32_f16 v[120:123], v[160:163], v[192:195], v[120:123]
	v_mfma_f32_16x16x32_f16 v[120:123], v[156:159], v[188:191], v[120:123]
	v_mfma_f32_16x16x32_f16 v[104:107], v[156:159], v[176:179], v[104:107]
	v_mfma_f32_16x16x32_f16 v[104:107], v[160:163], v[180:183], v[104:107]
	v_mfma_f32_16x16x32_f16 v[112:115], v[152:155], v[180:183], v[112:115]
	v_mfma_f32_16x16x32_f16 v[112:115], v[148:151], v[176:179], v[112:115]
	v_mfma_f32_16x16x32_f16 v[96:99], v[148:151], v[172:175], v[96:99]
	v_mfma_f32_16x16x32_f16 v[96:99], v[152:155], v[184:187], v[96:99]
	v_mfma_f32_16x16x32_f16 v[88:91], v[160:163], v[184:187], v[88:91]
	v_mfma_f32_16x16x32_f16 v[88:91], v[156:159], v[172:175], v[88:91]
	v_mfma_f32_16x16x32_f16 v[72:75], v[156:159], v[164:167], v[72:75]
	v_mfma_f32_16x16x32_f16 v[72:75], v[160:163], v[168:171], v[72:75]
	v_mfma_f32_16x16x32_f16 v[80:83], v[152:155], v[168:171], v[80:83]
	v_mfma_f32_16x16x32_f16 v[80:83], v[148:151], v[164:167], v[80:83]
	v_mfma_f32_16x16x32_f16 v[124:127], v[132:135], v[188:191], v[124:127]
	v_mfma_f32_16x16x32_f16 v[124:127], v[136:139], v[192:195], v[124:127]
	v_mfma_f32_16x16x32_f16 v[116:119], v[144:147], v[192:195], v[116:119]
	v_mfma_f32_16x16x32_f16 v[116:119], v[140:143], v[188:191], v[116:119]
	v_mfma_f32_16x16x32_f16 v[100:103], v[140:143], v[176:179], v[100:103]
	v_mfma_f32_16x16x32_f16 v[100:103], v[144:147], v[180:183], v[100:103]
	v_mfma_f32_16x16x32_f16 v[108:111], v[136:139], v[180:183], v[108:111]
	v_mfma_f32_16x16x32_f16 v[108:111], v[132:135], v[176:179], v[108:111]
	v_mfma_f32_16x16x32_f16 v[92:95], v[132:135], v[172:175], v[92:95]
	v_mfma_f32_16x16x32_f16 v[92:95], v[136:139], v[184:187], v[92:95]
	v_mfma_f32_16x16x32_f16 v[84:87], v[144:147], v[184:187], v[84:87]
	v_mfma_f32_16x16x32_f16 v[84:87], v[140:143], v[172:175], v[84:87]
	v_mfma_f32_16x16x32_f16 v[68:71], v[140:143], v[164:167], v[68:71]
	v_mfma_f32_16x16x32_f16 v[68:71], v[144:147], v[168:171], v[68:71]
	v_mfma_f32_16x16x32_f16 v[76:79], v[136:139], v[168:171], v[76:79]
	v_mfma_f32_16x16x32_f16 v[76:79], v[132:135], v[164:167], v[76:79]
	s_barrier
	s_mov_b32 m0, s59
	s_add_u32 s4, s46, 0x100080
	ds_read_b128 v[164:167], v226 offset:49152
	ds_read_b128 v[168:171], v226 offset:51200
	ds_read_b128 v[172:175], v227 offset:49152
	ds_read_b128 v[176:179], v227 offset:51200
	ds_read_b128 v[180:183], v226 offset:53248
	ds_read_b128 v[184:187], v226 offset:55296
	ds_read_b128 v[188:191], v227 offset:53248
	ds_read_b128 v[192:195], v227 offset:55296
	global_load_lds_dwordx4 v200, s[84:85] sc1
	s_mov_b32 m0, s60
	s_addc_u32 s5, s47, 0
	global_load_lds_dwordx4 v196, s[84:85] sc1
	s_mov_b32 m0, s63
	s_nop 0
	global_load_lds_dwordx4 v200, s[4:5] sc1
	s_mov_b32 m0, s64
	s_nop 0
	global_load_lds_dwordx4 v196, s[4:5] sc1
	s_mov_b32 m0, s61
	s_nop 0
	global_load_lds_dwordx4 v202, s[86:87] sc1
	s_mov_b32 m0, s62
	s_nop 0
	global_load_lds_dwordx4 v198, s[86:87] sc1
	s_waitcnt vmcnt(8)
	s_waitcnt lgkmcnt(0)
	s_barrier
	v_mfma_f32_16x16x32_f16 v[64:67], v[148:151], v[164:167], v[64:67]
	v_mfma_f32_16x16x32_f16 v[64:67], v[152:155], v[172:175], v[64:67]
	v_mfma_f32_16x16x32_f16 v[56:59], v[160:163], v[172:175], v[56:59]
	v_mfma_f32_16x16x32_f16 v[56:59], v[156:159], v[164:167], v[56:59]
	v_mfma_f32_16x16x32_f16 v[40:43], v[156:159], v[168:171], v[40:43]
	v_mfma_f32_16x16x32_f16 v[40:43], v[160:163], v[176:179], v[40:43]
	v_mfma_f32_16x16x32_f16 v[48:51], v[152:155], v[176:179], v[48:51]
	v_mfma_f32_16x16x32_f16 v[48:51], v[148:151], v[168:171], v[48:51]
	v_mfma_f32_16x16x32_f16 v[32:35], v[148:151], v[180:183], v[32:35]
	v_mfma_f32_16x16x32_f16 v[32:35], v[152:155], v[188:191], v[32:35]
	v_mfma_f32_16x16x32_f16 v[24:27], v[160:163], v[188:191], v[24:27]
	v_mfma_f32_16x16x32_f16 v[24:27], v[156:159], v[180:183], v[24:27]
	v_mfma_f32_16x16x32_f16 v[8:11], v[156:159], v[184:187], v[8:11]
	v_mfma_f32_16x16x32_f16 v[8:11], v[160:163], v[192:195], v[8:11]
	v_mfma_f32_16x16x32_f16 v[16:19], v[152:155], v[192:195], v[16:19]
	v_mfma_f32_16x16x32_f16 v[16:19], v[148:151], v[184:187], v[16:19]
	v_mfma_f32_16x16x32_f16 v[60:63], v[132:135], v[164:167], v[60:63]
	v_mfma_f32_16x16x32_f16 v[60:63], v[136:139], v[172:175], v[60:63]
	v_mfma_f32_16x16x32_f16 v[52:55], v[144:147], v[172:175], v[52:55]
	v_mfma_f32_16x16x32_f16 v[52:55], v[140:143], v[164:167], v[52:55]
	v_mfma_f32_16x16x32_f16 v[36:39], v[140:143], v[168:171], v[36:39]
	v_mfma_f32_16x16x32_f16 v[36:39], v[144:147], v[176:179], v[36:39]
	v_mfma_f32_16x16x32_f16 v[44:47], v[136:139], v[176:179], v[44:47]
	v_mfma_f32_16x16x32_f16 v[44:47], v[132:135], v[168:171], v[44:47]
	v_mfma_f32_16x16x32_f16 v[28:31], v[132:135], v[180:183], v[28:31]
	v_mfma_f32_16x16x32_f16 v[28:31], v[136:139], v[188:191], v[28:31]
	v_mfma_f32_16x16x32_f16 v[20:23], v[144:147], v[188:191], v[20:23]
	v_mfma_f32_16x16x32_f16 v[20:23], v[140:143], v[180:183], v[20:23]
	v_mfma_f32_16x16x32_f16 v[4:7], v[140:143], v[184:187], v[4:7]
	v_mfma_f32_16x16x32_f16 v[4:7], v[144:147], v[192:195], v[4:7]
	v_mfma_f32_16x16x32_f16 v[12:15], v[136:139], v[192:195], v[12:15]
	v_mfma_f32_16x16x32_f16 v[12:15], v[132:135], v[184:187], v[12:15]
	s_barrier
	s_add_u32 s80, s80, 0x100
	s_addc_u32 s81, s81, 0
	s_add_u32 s44, s44, 0x100
	s_addc_u32 s45, s45, 0
	s_cmp_gt_u32 s82, 61
	s_cbranch_scc1 .LBB1_4
	s_mov_b32 s48, s82
	s_branch .LBB1_9

.LBB2_20:
	s_add_u32 s30, s28, 0xffc80080
	s_addc_u32 s31, s29, -1
	s_cmpk_eq_i32 s58, 0xdc
	s_cselect_b32 s35, s25, s31
	s_cselect_b32 s34, s24, s30
	s_cselect_b32 s31, s27, s57
	s_cselect_b32 s30, s26, s56
	s_add_i32 m0, s37, 0xc000
	ds_read_b128 v[166:169], v143
	ds_read_b128 v[170:173], v147
	ds_read_b128 v[174:177], v149
	ds_read_b128 v[178:181], v150
	ds_read_b128 v[182:185], v151
	ds_read_b128 v[186:189], v152
	ds_read_b128 v[190:193], v153
	ds_read_b128 v[194:197], v154
	ds_read_b128 v[198:201], v155
	ds_read_b128 v[202:205], v155 offset:2048
	ds_read_b128 v[206:209], v156
	ds_read_b128 v[210:213], v156 offset:2048
	ds_read_b128 v[214:217], v155 offset:4096
	ds_read_b128 v[218:221], v155 offset:6144
	ds_read_b128 v[222:225], v156 offset:4096
	ds_read_b128 v[226:229], v156 offset:6144
	global_load_lds_dwordx4 v134, s[28:29] sc1
	s_add_i32 m0, s37, 0xe000
	s_nop 0
	global_load_lds_dwordx4 v132, s[28:29] sc1
	s_waitcnt vmcnt(8)
	s_waitcnt lgkmcnt(0)
	s_barrier
	v_mfma_f32_16x16x32_f16 v[124:127], v[166:169], v[198:201], v[124:127]
	v_mfma_f32_16x16x32_f16 v[124:127], v[170:173], v[206:209], v[124:127]
	v_mfma_f32_16x16x32_f16 v[120:123], v[178:181], v[206:209], v[120:123]
	v_mfma_f32_16x16x32_f16 v[120:123], v[174:177], v[198:201], v[120:123]
	v_mfma_f32_16x16x32_f16 v[112:115], v[174:177], v[202:205], v[112:115]
	v_mfma_f32_16x16x32_f16 v[112:115], v[178:181], v[210:213], v[112:115]
	v_mfma_f32_16x16x32_f16 v[116:119], v[170:173], v[210:213], v[116:119]
	v_mfma_f32_16x16x32_f16 v[116:119], v[166:169], v[202:205], v[116:119]
	v_mfma_f32_16x16x32_f16 v[108:111], v[166:169], v[214:217], v[108:111]
	v_mfma_f32_16x16x32_f16 v[108:111], v[170:173], v[222:225], v[108:111]
	v_mfma_f32_16x16x32_f16 v[100:103], v[178:181], v[222:225], v[100:103]
	v_mfma_f32_16x16x32_f16 v[100:103], v[174:177], v[214:217], v[100:103]
	v_mfma_f32_16x16x32_f16 v[84:87], v[174:177], v[218:221], v[84:87]
	v_mfma_f32_16x16x32_f16 v[84:87], v[178:181], v[226:229], v[84:87]
	v_mfma_f32_16x16x32_f16 v[92:95], v[170:173], v[226:229], v[92:95]
	v_mfma_f32_16x16x32_f16 v[92:95], v[166:169], v[218:221], v[92:95]
	v_mfma_f32_16x16x32_f16 v[104:107], v[182:185], v[198:201], v[104:107]
	v_mfma_f32_16x16x32_f16 v[104:107], v[186:189], v[206:209], v[104:107]
	v_mfma_f32_16x16x32_f16 v[96:99], v[194:197], v[206:209], v[96:99]
	v_mfma_f32_16x16x32_f16 v[96:99], v[190:193], v[198:201], v[96:99]
	v_mfma_f32_16x16x32_f16 v[80:83], v[190:193], v[202:205], v[80:83]
	v_mfma_f32_16x16x32_f16 v[80:83], v[194:197], v[210:213], v[80:83]
	v_mfma_f32_16x16x32_f16 v[88:91], v[186:189], v[210:213], v[88:91]
	v_mfma_f32_16x16x32_f16 v[88:91], v[182:185], v[202:205], v[88:91]
	v_mfma_f32_16x16x32_f16 v[76:79], v[182:185], v[214:217], v[76:79]
	v_mfma_f32_16x16x32_f16 v[76:79], v[186:189], v[222:225], v[76:79]
	v_mfma_f32_16x16x32_f16 v[72:75], v[194:197], v[222:225], v[72:75]
	v_mfma_f32_16x16x32_f16 v[72:75], v[190:193], v[214:217], v[72:75]
	v_mfma_f32_16x16x32_f16 v[64:67], v[190:193], v[218:221], v[64:67]
	v_mfma_f32_16x16x32_f16 v[64:67], v[194:197], v[226:229], v[64:67]
	v_mfma_f32_16x16x32_f16 v[68:71], v[186:189], v[226:229], v[68:71]
	v_mfma_f32_16x16x32_f16 v[68:71], v[182:185], v[218:221], v[68:71]
	s_barrier
	s_add_i32 s59, s43, s36
	s_mov_b32 m0, s59
	ds_read_b128 v[198:201], v155 offset:16384
	ds_read_b128 v[202:205], v155 offset:18432
	ds_read_b128 v[206:209], v156 offset:16384
	ds_read_b128 v[210:213], v156 offset:18432
	ds_read_b128 v[214:217], v155 offset:20480
	ds_read_b128 v[218:221], v155 offset:22528
	ds_read_b128 v[222:225], v156 offset:20480
	ds_read_b128 v[226:229], v156 offset:22528
	global_load_lds_dwordx4 v128, s[30:31] sc1
	s_add_i32 m0, s59, 0x2000
	s_add_u32 s60, s30, 0x380000
	s_addc_u32 s61, s31, 0
	s_add_i32 s59, s44, s36
	global_load_lds_dwordx4 v130, s[30:31] sc1
	s_mov_b32 m0, s59
	s_add_u32 s62, s30, 0x80
	s_addc_u32 s63, s31, 0
	global_load_lds_dwordx4 v128, s[60:61] sc1
	s_add_i32 m0, s59, 0x2000
	s_add_u32 s64, s34, 0x80
	s_addc_u32 s65, s35, 0
	global_load_lds_dwordx4 v130, s[60:61] sc1
	s_mov_b32 m0, s37
	s_nop 0
	global_load_lds_dwordx4 v128, s[34:35] sc1
	s_mov_b32 m0, s38
	s_nop 0
	global_load_lds_dwordx4 v130, s[34:35] sc1
	s_waitcnt vmcnt(8)
	s_waitcnt lgkmcnt(0)
	s_barrier
	v_mfma_f32_16x16x32_f16 v[60:63], v[166:169], v[198:201], v[60:63]
	v_mfma_f32_16x16x32_f16 v[60:63], v[170:173], v[206:209], v[60:63]
	v_mfma_f32_16x16x32_f16 v[56:59], v[178:181], v[206:209], v[56:59]
	v_mfma_f32_16x16x32_f16 v[56:59], v[174:177], v[198:201], v[56:59]
	v_mfma_f32_16x16x32_f16 v[48:51], v[174:177], v[202:205], v[48:51]
	v_mfma_f32_16x16x32_f16 v[48:51], v[178:181], v[210:213], v[48:51]
	v_mfma_f32_16x16x32_f16 v[52:55], v[170:173], v[210:213], v[52:55]
	v_mfma_f32_16x16x32_f16 v[52:55], v[166:169], v[202:205], v[52:55]
	v_mfma_f32_16x16x32_f16 v[40:43], v[166:169], v[214:217], v[40:43]
	v_mfma_f32_16x16x32_f16 v[40:43], v[170:173], v[222:225], v[40:43]
	v_mfma_f32_16x16x32_f16 v[32:35], v[178:181], v[222:225], v[32:35]
	v_mfma_f32_16x16x32_f16 v[32:35], v[174:177], v[214:217], v[32:35]
	v_mfma_f32_16x16x32_f16 v[8:11], v[174:177], v[218:221], v[8:11]
	v_mfma_f32_16x16x32_f16 v[8:11], v[178:181], v[226:229], v[8:11]
	v_mfma_f32_16x16x32_f16 v[12:15], v[170:173], v[226:229], v[12:15]
	v_mfma_f32_16x16x32_f16 v[12:15], v[166:169], v[218:221], v[12:15]
	v_mfma_f32_16x16x32_f16 v[44:47], v[182:185], v[198:201], v[44:47]
	v_mfma_f32_16x16x32_f16 v[44:47], v[186:189], v[206:209], v[44:47]
	v_mfma_f32_16x16x32_f16 v[36:39], v[194:197], v[206:209], v[36:39]
	v_mfma_f32_16x16x32_f16 v[36:39], v[190:193], v[198:201], v[36:39]
	v_mfma_f32_16x16x32_f16 v[24:27], v[190:193], v[202:205], v[24:27]
	v_mfma_f32_16x16x32_f16 v[24:27], v[194:197], v[210:213], v[24:27]
	v_mfma_f32_16x16x32_f16 v[28:31], v[186:189], v[210:213], v[28:31]
	v_mfma_f32_16x16x32_f16 v[28:31], v[182:185], v[202:205], v[28:31]
	v_mfma_f32_16x16x32_f16 v[20:23], v[182:185], v[214:217], v[20:23]
	v_mfma_f32_16x16x32_f16 v[20:23], v[186:189], v[222:225], v[20:23]
	v_mfma_f32_16x16x32_f16 v[16:19], v[194:197], v[222:225], v[16:19]
	v_mfma_f32_16x16x32_f16 v[16:19], v[190:193], v[214:217], v[16:19]
	v_mfma_f32_16x16x32_f16 v[0:3], v[190:193], v[218:221], v[0:3]
	v_mfma_f32_16x16x32_f16 v[0:3], v[194:197], v[226:229], v[0:3]
	v_mfma_f32_16x16x32_f16 v[4:7], v[186:189], v[226:229], v[4:7]
	v_mfma_f32_16x16x32_f16 v[4:7], v[182:185], v[218:221], v[4:7]
	s_barrier
	s_add_u32 s34, s34, 0x380000
	s_addc_u32 s35, s35, 0
	s_mov_b32 m0, s39
	ds_read_b128 v[166:169], v157
	ds_read_b128 v[170:173], v158
	ds_read_b128 v[174:177], v159
	ds_read_b128 v[178:181], v160
	ds_read_b128 v[182:185], v161
	ds_read_b128 v[186:189], v162
	ds_read_b128 v[190:193], v163
	ds_read_b128 v[194:197], v164
	ds_read_b128 v[198:201], v155 offset:32768
	ds_read_b128 v[202:205], v155 offset:34816
	ds_read_b128 v[206:209], v156 offset:32768
	ds_read_b128 v[210:213], v156 offset:34816
	ds_read_b128 v[214:217], v155 offset:36864
	ds_read_b128 v[218:221], v155 offset:38912
	ds_read_b128 v[222:225], v156 offset:36864
	ds_read_b128 v[226:229], v156 offset:38912
	global_load_lds_dwordx4 v128, s[34:35] sc1
	s_mov_b32 m0, s40
	s_nop 0
	global_load_lds_dwordx4 v130, s[34:35] sc1
	s_waitcnt vmcnt(8)
	s_waitcnt lgkmcnt(0)
	s_barrier
	v_mfma_f32_16x16x32_f16 v[124:127], v[166:169], v[198:201], v[124:127]
	v_mfma_f32_16x16x32_f16 v[124:127], v[170:173], v[206:209], v[124:127]
	v_mfma_f32_16x16x32_f16 v[120:123], v[178:181], v[206:209], v[120:123]
	v_mfma_f32_16x16x32_f16 v[120:123], v[174:177], v[198:201], v[120:123]
	v_mfma_f32_16x16x32_f16 v[112:115], v[174:177], v[202:205], v[112:115]
	v_mfma_f32_16x16x32_f16 v[112:115], v[178:181], v[210:213], v[112:115]
	v_mfma_f32_16x16x32_f16 v[116:119], v[170:173], v[210:213], v[116:119]
	v_mfma_f32_16x16x32_f16 v[116:119], v[166:169], v[202:205], v[116:119]
	v_mfma_f32_16x16x32_f16 v[108:111], v[166:169], v[214:217], v[108:111]
	v_mfma_f32_16x16x32_f16 v[108:111], v[170:173], v[222:225], v[108:111]
	v_mfma_f32_16x16x32_f16 v[100:103], v[178:181], v[222:225], v[100:103]
	v_mfma_f32_16x16x32_f16 v[100:103], v[174:177], v[214:217], v[100:103]
	v_mfma_f32_16x16x32_f16 v[84:87], v[174:177], v[218:221], v[84:87]
	v_mfma_f32_16x16x32_f16 v[84:87], v[178:181], v[226:229], v[84:87]
	v_mfma_f32_16x16x32_f16 v[92:95], v[170:173], v[226:229], v[92:95]
	v_mfma_f32_16x16x32_f16 v[92:95], v[166:169], v[218:221], v[92:95]
	v_mfma_f32_16x16x32_f16 v[104:107], v[182:185], v[198:201], v[104:107]
	v_mfma_f32_16x16x32_f16 v[104:107], v[186:189], v[206:209], v[104:107]
	v_mfma_f32_16x16x32_f16 v[96:99], v[194:197], v[206:209], v[96:99]
	v_mfma_f32_16x16x32_f16 v[96:99], v[190:193], v[198:201], v[96:99]
	v_mfma_f32_16x16x32_f16 v[80:83], v[190:193], v[202:205], v[80:83]
	v_mfma_f32_16x16x32_f16 v[80:83], v[194:197], v[210:213], v[80:83]
	v_mfma_f32_16x16x32_f16 v[88:91], v[186:189], v[210:213], v[88:91]
	v_mfma_f32_16x16x32_f16 v[88:91], v[182:185], v[202:205], v[88:91]
	v_mfma_f32_16x16x32_f16 v[76:79], v[182:185], v[214:217], v[76:79]
	v_mfma_f32_16x16x32_f16 v[76:79], v[186:189], v[222:225], v[76:79]
	v_mfma_f32_16x16x32_f16 v[72:75], v[194:197], v[222:225], v[72:75]
	v_mfma_f32_16x16x32_f16 v[72:75], v[190:193], v[214:217], v[72:75]
	v_mfma_f32_16x16x32_f16 v[64:67], v[190:193], v[218:221], v[64:67]
	v_mfma_f32_16x16x32_f16 v[64:67], v[194:197], v[226:229], v[64:67]
	v_mfma_f32_16x16x32_f16 v[68:71], v[186:189], v[226:229], v[68:71]
	v_mfma_f32_16x16x32_f16 v[68:71], v[182:185], v[218:221], v[68:71]
	s_barrier
	s_add_i32 s34, s46, s36
	s_mov_b32 m0, s34
	ds_read_b128 v[198:201], v155 offset:49152
	ds_read_b128 v[202:205], v155 offset:51200
	ds_read_b128 v[206:209], v156 offset:49152
	ds_read_b128 v[210:213], v156 offset:51200
	ds_read_b128 v[214:217], v155 offset:53248
	ds_read_b128 v[218:221], v155 offset:55296
	ds_read_b128 v[222:225], v156 offset:53248
	ds_read_b128 v[226:229], v156 offset:55296
	global_load_lds_dwordx4 v128, s[62:63] sc1
	s_add_i32 m0, s34, 0x2000
	s_add_u32 s30, s30, 0x380080
	s_addc_u32 s31, s31, 0
	s_add_i32 s34, s47, s36
	global_load_lds_dwordx4 v130, s[62:63] sc1
	s_mov_b32 m0, s34
	s_nop 0
	global_load_lds_dwordx4 v128, s[30:31] sc1
	s_add_i32 m0, s34, 0x2000
	s_nop 0
	global_load_lds_dwordx4 v130, s[30:31] sc1
	s_mov_b32 m0, s41
	s_nop 0
	global_load_lds_dwordx4 v128, s[64:65] sc1
	s_mov_b32 m0, s42
	s_nop 0
	global_load_lds_dwordx4 v130, s[64:65] sc1
	s_waitcnt vmcnt(8)
	s_waitcnt lgkmcnt(0)
	s_barrier
	v_mfma_f32_16x16x32_f16 v[60:63], v[166:169], v[198:201], v[60:63]
	v_mfma_f32_16x16x32_f16 v[60:63], v[170:173], v[206:209], v[60:63]
	v_mfma_f32_16x16x32_f16 v[56:59], v[178:181], v[206:209], v[56:59]
	v_mfma_f32_16x16x32_f16 v[56:59], v[174:177], v[198:201], v[56:59]
	v_mfma_f32_16x16x32_f16 v[48:51], v[174:177], v[202:205], v[48:51]
	v_mfma_f32_16x16x32_f16 v[48:51], v[178:181], v[210:213], v[48:51]
	v_mfma_f32_16x16x32_f16 v[52:55], v[170:173], v[210:213], v[52:55]
	v_mfma_f32_16x16x32_f16 v[52:55], v[166:169], v[202:205], v[52:55]
	v_mfma_f32_16x16x32_f16 v[40:43], v[166:169], v[214:217], v[40:43]
	v_mfma_f32_16x16x32_f16 v[40:43], v[170:173], v[222:225], v[40:43]
	v_mfma_f32_16x16x32_f16 v[32:35], v[178:181], v[222:225], v[32:35]
	v_mfma_f32_16x16x32_f16 v[32:35], v[174:177], v[214:217], v[32:35]
	v_mfma_f32_16x16x32_f16 v[8:11], v[174:177], v[218:221], v[8:11]
	v_mfma_f32_16x16x32_f16 v[8:11], v[178:181], v[226:229], v[8:11]
	v_mfma_f32_16x16x32_f16 v[12:15], v[170:173], v[226:229], v[12:15]
	v_mfma_f32_16x16x32_f16 v[12:15], v[166:169], v[218:221], v[12:15]
	v_mfma_f32_16x16x32_f16 v[44:47], v[182:185], v[198:201], v[44:47]
	v_mfma_f32_16x16x32_f16 v[44:47], v[186:189], v[206:209], v[44:47]
	v_mfma_f32_16x16x32_f16 v[36:39], v[194:197], v[206:209], v[36:39]
	v_mfma_f32_16x16x32_f16 v[36:39], v[190:193], v[198:201], v[36:39]
	v_mfma_f32_16x16x32_f16 v[24:27], v[190:193], v[202:205], v[24:27]
	v_mfma_f32_16x16x32_f16 v[24:27], v[194:197], v[210:213], v[24:27]
	v_mfma_f32_16x16x32_f16 v[28:31], v[186:189], v[210:213], v[28:31]
	v_mfma_f32_16x16x32_f16 v[28:31], v[182:185], v[202:205], v[28:31]
	v_mfma_f32_16x16x32_f16 v[20:23], v[182:185], v[214:217], v[20:23]
	v_mfma_f32_16x16x32_f16 v[20:23], v[186:189], v[222:225], v[20:23]
	v_mfma_f32_16x16x32_f16 v[16:19], v[194:197], v[222:225], v[16:19]
	v_mfma_f32_16x16x32_f16 v[16:19], v[190:193], v[214:217], v[16:19]
	v_mfma_f32_16x16x32_f16 v[0:3], v[190:193], v[218:221], v[0:3]
	v_mfma_f32_16x16x32_f16 v[0:3], v[194:197], v[226:229], v[0:3]
	v_mfma_f32_16x16x32_f16 v[4:7], v[186:189], v[226:229], v[4:7]
	v_mfma_f32_16x16x32_f16 v[4:7], v[182:185], v[218:221], v[4:7]
	s_barrier
	s_add_i32 s58, s58, 2
	s_add_u32 s56, s56, 0x100
	s_addc_u32 s57, s57, 0
	s_add_u32 s28, s28, 0x100
	s_addc_u32 s29, s29, 0
	s_cmpk_gt_u32 s58, 0xdd
	s_cbranch_scc0 .LBB2_20
	v_lshl_add_u32 v144, s55, 8, v137
	v_ashrrev_i32_e32 v145, 31, v144
	v_lshl_add_u64 v[138:139], v[144:145], 2, s[10:11]
	global_load_dword v136, v[138:139], off
	global_load_dword v140, v[138:139], off offset:64
	global_load_dword v142, v[138:139], off offset:128
	global_load_dword v146, v[138:139], off offset:192
	global_load_dword v148, v[138:139], off offset:512
	global_load_dword v174, v[138:139], off offset:576
	global_load_dword v176, v[138:139], off offset:640
	s_nop 0
	global_load_dword v138, v[138:139], off offset:704
	v_lshl_or_b32 v166, s54, 8, v141
	v_ashrrev_i32_e32 v167, 31, v166
	v_or_b32_e32 v168, 16, v144
	v_or_b32_e32 v170, 32, v144
	v_or_b32_e32 v172, 48, v144
	v_lshl_add_u64 v[166:167], v[166:167], 2, s[8:9]
	v_lshlrev_b64 v[144:145], 14, v[144:145]
	v_ashrrev_i32_e32 v169, 31, v168
	v_ashrrev_i32_e32 v171, 31, v170
	v_ashrrev_i32_e32 v173, 31, v172
	v_lshl_add_u64 v[144:145], v[166:167], 0, v[144:145]
	v_lshlrev_b64 v[168:169], 14, v[168:169]
	v_lshlrev_b64 v[170:171], 14, v[170:171]
	v_lshlrev_b64 v[172:173], 14, v[172:173]
	v_add_co_u32_e32 v178, vcc, s48, v144
	v_lshl_add_u64 v[168:169], v[166:167], 0, v[168:169]
	v_lshl_add_u64 v[170:171], v[166:167], 0, v[170:171]
	v_lshl_add_u64 v[166:167], v[166:167], 0, v[172:173]
	v_lshl_add_u64 v[172:173], v[144:145], 0, s[16:17]
	v_addc_co_u32_e32 v179, vcc, 0, v145, vcc
	s_mov_b32 s55, s45
	s_mov_b32 s54, s53
	s_mov_b64 s[28:29], s[26:27]
	s_mov_b64 s[30:31], s[24:25]
	s_waitcnt vmcnt(0)
	v_pk_mul_f32 v[126:127], v[136:137], v[126:127] op_sel_hi:[0,1]
	v_pk_mul_f32 v[124:125], v[136:137], v[124:125] op_sel_hi:[0,1]
	v_pk_mul_f32 v[122:123], v[136:137], v[122:123] op_sel_hi:[0,1]
	v_pk_mul_f32 v[120:121], v[136:137], v[120:121] op_sel_hi:[0,1]
	v_pk_mul_f32 v[46:47], v[148:149], v[46:47] op_sel_hi:[0,1]
	v_pk_mul_f32 v[44:45], v[148:149], v[44:45] op_sel_hi:[0,1]
	v_pk_mul_f32 v[106:107], v[136:137], v[106:107] op_sel_hi:[0,1]
	v_pk_mul_f32 v[104:105], v[136:137], v[104:105] op_sel_hi:[0,1]
	v_pk_mul_f32 v[98:99], v[136:137], v[98:99] op_sel_hi:[0,1]
	v_pk_mul_f32 v[96:97], v[136:137], v[96:97] op_sel_hi:[0,1]
	v_pk_mul_f32 v[118:119], v[140:141], v[118:119] op_sel_hi:[0,1]
	v_pk_mul_f32 v[116:117], v[140:141], v[116:117] op_sel_hi:[0,1]
	v_pk_mul_f32 v[114:115], v[140:141], v[114:115] op_sel_hi:[0,1]
	v_pk_mul_f32 v[112:113], v[140:141], v[112:113] op_sel_hi:[0,1]
	v_pk_mul_f32 v[90:91], v[140:141], v[90:91] op_sel_hi:[0,1]
	v_pk_mul_f32 v[88:89], v[140:141], v[88:89] op_sel_hi:[0,1]
	v_pk_mul_f32 v[82:83], v[140:141], v[82:83] op_sel_hi:[0,1]
	v_pk_mul_f32 v[80:81], v[140:141], v[80:81] op_sel_hi:[0,1]
	v_pk_mul_f32 v[110:111], v[142:143], v[110:111] op_sel_hi:[0,1]
	v_pk_mul_f32 v[108:109], v[142:143], v[108:109] op_sel_hi:[0,1]
	v_pk_mul_f32 v[102:103], v[142:143], v[102:103] op_sel_hi:[0,1]
	v_pk_mul_f32 v[100:101], v[142:143], v[100:101] op_sel_hi:[0,1]
	v_pk_mul_f32 v[78:79], v[142:143], v[78:79] op_sel_hi:[0,1]
	v_pk_mul_f32 v[76:77], v[142:143], v[76:77] op_sel_hi:[0,1]
	v_pk_mul_f32 v[74:75], v[142:143], v[74:75] op_sel_hi:[0,1]
	v_pk_mul_f32 v[72:73], v[142:143], v[72:73] op_sel_hi:[0,1]
	v_pk_mul_f32 v[94:95], v[146:147], v[94:95] op_sel_hi:[0,1]
	v_pk_mul_f32 v[92:93], v[146:147], v[92:93] op_sel_hi:[0,1]
	v_pk_mul_f32 v[86:87], v[146:147], v[86:87] op_sel_hi:[0,1]
	v_pk_mul_f32 v[84:85], v[146:147], v[84:85] op_sel_hi:[0,1]
	v_pk_mul_f32 v[70:71], v[146:147], v[70:71] op_sel_hi:[0,1]
	v_pk_mul_f32 v[68:69], v[146:147], v[68:69] op_sel_hi:[0,1]
	v_pk_mul_f32 v[66:67], v[146:147], v[66:67] op_sel_hi:[0,1]
	v_pk_mul_f32 v[64:65], v[146:147], v[64:65] op_sel_hi:[0,1]
	v_pk_mul_f32 v[62:63], v[148:149], v[62:63] op_sel_hi:[0,1]
	v_pk_mul_f32 v[60:61], v[148:149], v[60:61] op_sel_hi:[0,1]
	global_store_dwordx4 v[144:145], v[124:127], off nt
	global_store_dwordx4 v[144:145], v[120:123], off offset:64 nt
	global_store_dwordx4 v[144:145], v[104:107], off offset:512 nt
	global_store_dwordx4 v[144:145], v[96:99], off offset:576 nt
	global_store_dwordx4 v[168:169], v[116:119], off nt
	global_store_dwordx4 v[168:169], v[112:115], off offset:64 nt
	global_store_dwordx4 v[168:169], v[88:91], off offset:512 nt
	global_store_dwordx4 v[168:169], v[80:83], off offset:576 nt
	global_store_dwordx4 v[170:171], v[108:111], off nt
	global_store_dwordx4 v[170:171], v[100:103], off offset:64 nt
	global_store_dwordx4 v[170:171], v[76:79], off offset:512 nt
	global_store_dwordx4 v[170:171], v[72:75], off offset:576 nt
	global_store_dwordx4 v[166:167], v[92:95], off nt
	global_store_dwordx4 v[166:167], v[84:87], off offset:64 nt
	global_store_dwordx4 v[166:167], v[68:71], off offset:512 nt
	global_store_dwordx4 v[166:167], v[64:67], off offset:576 nt
	global_store_dwordx4 v[178:179], v[60:63], off nt
	global_store_dwordx4 v[172:173], v[44:47], off offset:512 nt
	v_pk_mul_f32 v[30:31], v[174:175], v[30:31] op_sel_hi:[0,1]
	v_pk_mul_f32 v[28:29], v[174:175], v[28:29] op_sel_hi:[0,1]
	v_add_co_u32_e32 v46, vcc, s49, v144
	v_lshl_add_u64 v[44:45], v[144:145], 0, s[18:19]
	s_nop 0
	v_addc_co_u32_e32 v47, vcc, 0, v145, vcc
	global_store_dwordx4 v[44:45], v[28:31], off offset:512 nt
	v_pk_mul_f32 v[18:19], v[176:177], v[18:19] op_sel_hi:[0,1]
	v_pk_mul_f32 v[16:17], v[176:177], v[16:17] op_sel_hi:[0,1]
	v_add_co_u32_e32 v30, vcc, s50, v144
	v_lshl_add_u64 v[28:29], v[144:145], 0, s[20:21]
	s_nop 0
	v_addc_co_u32_e32 v31, vcc, 0, v145, vcc
	v_pk_mul_f32 v[38:39], v[148:149], v[38:39] op_sel_hi:[0,1]
	v_pk_mul_f32 v[36:37], v[148:149], v[36:37] op_sel_hi:[0,1]
	v_pk_mul_f32 v[26:27], v[174:175], v[26:27] op_sel_hi:[0,1]
	v_pk_mul_f32 v[24:25], v[174:175], v[24:25] op_sel_hi:[0,1]
	global_store_dwordx4 v[28:29], v[16:19], off offset:576 nt
	global_store_dwordx4 v[172:173], v[36:39], off offset:576 nt
	global_store_dwordx4 v[44:45], v[24:27], off offset:576 nt
	v_add_co_u32_e32 v18, vcc, s51, v144
	v_pk_mul_f32 v[38:39], v[174:175], v[54:55] op_sel_hi:[0,1]
	v_pk_mul_f32 v[36:37], v[174:175], v[52:53] op_sel_hi:[0,1]
	v_pk_mul_f32 v[26:27], v[176:177], v[42:43] op_sel_hi:[0,1]
	v_pk_mul_f32 v[24:25], v[176:177], v[40:41] op_sel_hi:[0,1]
	v_addc_co_u32_e32 v19, vcc, 0, v145, vcc
	v_pk_mul_f32 v[58:59], v[148:149], v[58:59] op_sel_hi:[0,1]
	v_pk_mul_f32 v[56:57], v[148:149], v[56:57] op_sel_hi:[0,1]
	global_store_dwordx4 v[46:47], v[36:39], off nt
	global_store_dwordx4 v[30:31], v[24:27], off nt
	v_pk_mul_f32 v[22:23], v[176:177], v[22:23] op_sel_hi:[0,1]
	v_pk_mul_f32 v[38:39], v[174:175], v[50:51] op_sel_hi:[0,1]
	v_pk_mul_f32 v[36:37], v[174:175], v[48:49] op_sel_hi:[0,1]
	v_pk_mul_f32 v[26:27], v[176:177], v[34:35] op_sel_hi:[0,1]
	v_pk_mul_f32 v[24:25], v[176:177], v[32:33] op_sel_hi:[0,1]
	v_pk_mul_f32 v[20:21], v[176:177], v[20:21] op_sel_hi:[0,1]
	v_lshl_add_u64 v[16:17], v[144:145], 0, s[22:23]
	v_pk_mul_f32 v[14:15], v[138:139], v[14:15] op_sel_hi:[0,1]
	v_pk_mul_f32 v[12:13], v[138:139], v[12:13] op_sel_hi:[0,1]
	v_pk_mul_f32 v[10:11], v[138:139], v[10:11] op_sel_hi:[0,1]
	v_pk_mul_f32 v[8:9], v[138:139], v[8:9] op_sel_hi:[0,1]
	v_pk_mul_f32 v[6:7], v[138:139], v[6:7] op_sel_hi:[0,1]
	v_pk_mul_f32 v[4:5], v[138:139], v[4:5] op_sel_hi:[0,1]
	v_pk_mul_f32 v[2:3], v[138:139], v[2:3] op_sel_hi:[0,1]
	v_pk_mul_f32 v[0:1], v[138:139], v[0:1] op_sel_hi:[0,1]
	s_mov_b64 vcc, s[0:1]
	global_store_dwordx4 v[172:173], v[56:59], off offset:64 nt
	global_store_dwordx4 v[44:45], v[36:39], off offset:64 nt
	global_store_dwordx4 v[28:29], v[24:27], off offset:64 nt
	global_store_dwordx4 v[28:29], v[20:23], off offset:512 nt
	global_store_dwordx4 v[18:19], v[12:15], off nt
	global_store_dwordx4 v[16:17], v[8:11], off offset:64 nt
	global_store_dwordx4 v[16:17], v[4:7], off offset:512 nt
	global_store_dwordx4 v[16:17], v[0:3], off offset:576 nt
	s_cbranch_vccz .LBB2_8
	s_waitcnt vmcnt(0)
	s_cmpk_gt_u32 s33, 0xff
	s_cbranch_scc1 .LBB2_24
	s_barrier
